# stack6 + cooperative L2 touch of the A row panel in the in-proj and out-proj GEMMs (current unit K-tiles t+4,t+5, then the next unit's first four)
# baseline (speedup 1.0000x reference)
; template <class Epi, class Sched>
; __device__ __forceinline__ void gemm_phase(LAS unsigned char* lds, const Sched& S, const Epi& E, const int wid) {
;     ...
;         for (int t = 0; t < nt; t += 2) {
;             const bool last = (t == nt - 2);
;             const char* a1 = cA + (size_t)(t + 1) * kstep;
;             const char* a2 = last ? nA : cA + (size_t)(t + 2) * kstep; const char* b2 = last ? nB : cB + (size_t)(t + 2) * kstep;
;             const char* a3 = a2 + kstep; const char* b3 = b2 + kstep;
.LBB7_219:
	s_cmp_gt_u32 s94, 1
	s_cbranch_scc1 .Lp1_notouch
	s_sub_i32 s100, s75, 10
	s_lshl_b32 s100, s100, 7
	s_cmp_gt_i32 s75, 8
	s_cselect_b32 s98, s36, s44
	s_cselect_b32 s99, s5, s45
	s_cselect_b32 s100, s100, 0x200
	s_add_u32 s98, s98, s100
	s_addc_u32 s99, s99, 0
	s_lshl_b32 s100, s94, 7
	s_add_u32 s98, s98, s100
	s_addc_u32 s99, s99, 0
	s_lshr_b32 s100, s92, 6
	s_and_b32 s100, s100, 3
	s_lshl_b32 s100, s100, 6
	v_mbcnt_lo_u32_b32 v210, -1, 0
	v_mbcnt_hi_u32_b32 v210, -1, v210
	v_add_u32_e32 v210, s100, v210
	v_lshlrev_b32_e32 v210, 11, v210
	global_load_dword v211, v210, s[98:99]

; template <class Epi, class Sched>
; __device__ __forceinline__ void gemm_phase(LAS unsigned char* lds, const Sched& S, const Epi& E, const int wid) {
;     ...
;         for (int t = 0; t < nt; t += 2) {
;             const bool last = (t == nt - 2);
;             const char* a1 = cA + (size_t)(t + 1) * kstep;
;             const char* a2 = last ? nA : cA + (size_t)(t + 2) * kstep; const char* b2 = last ? nB : cB + (size_t)(t + 2) * kstep;
;             const char* a3 = a2 + kstep; const char* b3 = b2 + kstep;
.LBB7_627:
	s_cmp_gt_u32 s94, 1
	s_cbranch_scc1 .Lp3_notouch
	s_sub_i32 s100, s81, 10
	s_lshl_b32 s100, s100, 7
	s_cmp_gt_i32 s81, 8
	s_cselect_b32 s98, s77, s46
	s_cselect_b32 s99, s39, s47
	s_cselect_b32 s100, s100, 0x200
	s_add_u32 s98, s98, s100
	s_addc_u32 s99, s99, 0
	s_lshl_b32 s100, s94, 7
	s_add_u32 s98, s98, s100
	s_addc_u32 s99, s99, 0
	s_lshr_b32 s100, s92, 6
	s_and_b32 s100, s100, 3
	s_lshl_b32 s100, s100, 6
	v_mbcnt_lo_u32_b32 v206, -1, 0
	v_mbcnt_hi_u32_b32 v206, -1, v206
	v_add_u32_e32 v206, s100, v206
	v_lshlrev_b32_e32 v206, 11, v206
	global_load_dword v207, v206, s[98:99]
